# stack17 = stack16 + QKV 1024-column passes: first K trip peeled with literal-zero C operand, the 128 v_mov accumulator zeroing per pass dropped
# baseline (speedup 1.0000x reference)
; #define REP(n) _Pragma("unroll 1") for (int rep_ = 0; rep_ < (n); ++rep_)
; #define LOADB(dst, ks_) do { const unsigned char* ub_ = wb + (size_t)((ks_) * 144) * 1024; \
;         _Pragma("unroll") for (int j_ = 0; j_ < 8; ++j_) dst[j_] = *(const bf16x8*)(ub_ + j_ * 1024 + voff); } while (0)
; #define LOADA(fd, ks_) do { _Pragma("unroll") for (int mi_ = 0; mi_ < 4; ++mi_) fd[mi_] = AFRAG(mi_, ks_); } while (0)
; #define MMA(src, fs, ksn_) do { _Pragma("unroll") for (int mi_ = 0; mi_ < 4; ++mi_) { \
;         _Pragma("unroll") for (int j_ = 0; j_ < 8; ++j_) acc[j_][mi_] = __builtin_amdgcn_mfma_f32_16x16x32_bf16(src[j_], fs[mi_], acc[j_][mi_], 0, 0, 0); \
;         fs[mi_] = AFRAG(mi_, (ksn_) < 32 ? (ksn_) : 31); } } while (0)
; #define LOADB(dst, ks_) do { const unsigned char* ub_ = wb + (size_t)((ks_) * 64) * 1024; \
;         _Pragma("unroll") for (int j_ = 0; j_ < 8; ++j_) dst[j_] = *(const bf16x8*)(ub_ + j_ * 1024 + voff); } while (0)
; #define LOADA(fd, ks_) do { _Pragma("unroll") for (int mi_ = 0; mi_ < 4; ++mi_) fd[mi_] = AFRAG(mi_, ks_); } while (0)
; DEVINL void phase2(const Params& P, unsigned char* smem, XPre& X, const bool have_pre) {
;     ...
;             REP(P2_RK) {
; #pragma unroll
;             for (int i = 0; i < 8; ++i)
; #pragma unroll
;                 for (int mi = 0; mi < 4; ++mi) acc[i][mi] = (f32x4){0.f, 0.f, 0.f, 0.f};
;             if (!SKIPF(256)) {
;                 const unsigned char* wb = (const unsigned char*)(P.ws + WS_WQF) + (size_t)(64 * pass + 8 * wv) * 1024;
;                 bf16x8 b0[8], b1[8];
;     ...
;                 bf16x8 fa[4];
;                 LOADB(b0, 0); LOADA(fa, 0);
; #pragma unroll 1
;                 for (int ks = 0; ks < 32; ks += 2) {
;                     LOADB(b1, ks + 1);
;                     __builtin_amdgcn_sched_barrier(0);
;                     MMA(b0, fa, ks + 1);
;                     __builtin_amdgcn_sched_barrier(0);
;                     LOADB(b0, ks + 2 < 32 ? ks + 2 : 31);
;                     __builtin_amdgcn_sched_barrier(0);
;                     MMA(b1, fa, ks + 2);
;                     __builtin_amdgcn_sched_barrier(0);
;                 }
.LBB0_203:
	s_and_b64 vcc, exec, s[0:1]
	s_cbranch_vccz .LBB0_190
	s_mov_b32 s0, 0
	s_and_b64 vcc, exec, s[86:87]
	s_cbranch_vccz .LBB0_208
	s_lshl_b32 s1, s8, 6
	s_add_i32 s6, s1, s3
	s_ashr_i32 s7, s6, 31
	s_lshl_b64 s[6:7], s[6:7], 10
	v_lshl_add_u64 v[200:201], v[194:195], 0, s[6:7]
	v_add_co_u32_e32 v2, vcc, 0x1000, v200
	global_load_dwordx4 v[130:133], v[200:201], off
	global_load_dwordx4 v[134:137], v[200:201], off offset:1024
	global_load_dwordx4 v[138:141], v[200:201], off offset:2048
	global_load_dwordx4 v[142:145], v[200:201], off offset:3072
	v_addc_co_u32_e32 v3, vcc, 0, v201, vcc
	global_load_dwordx4 v[158:161], v[2:3], off
	global_load_dwordx4 v[154:157], v[2:3], off offset:1024
	global_load_dwordx4 v[150:153], v[2:3], off offset:2048
	global_load_dwordx4 v[146:149], v[2:3], off offset:3072
	s_waitcnt lgkmcnt(3)
	ds_read_b128 v[174:177], v213
	s_waitcnt lgkmcnt(3)
	ds_read_b128 v[170:173], v213 offset:32768
	s_waitcnt lgkmcnt(3)
	ds_read_b128 v[166:169], v214
	s_waitcnt lgkmcnt(3)
	ds_read_b128 v[162:165], v215
	v_lshl_add_u64 v[202:203], v[198:199], 0, s[6:7]
	v_mov_b32_e32 v178, v217
	s_mov_b64 s[6:7], 0x1000
	v_lshl_add_u64 v[202:203], v[202:203], 0, s[6:7]
	global_load_dwordx4 v[218:221], v[202:203], off offset:-4096
	global_load_dwordx4 v[222:225], v[202:203], off offset:-3072
	global_load_dwordx4 v[226:229], v[202:203], off offset:-2048
	global_load_dwordx4 v[230:233], v[202:203], off offset:-1024
	global_load_dwordx4 v[234:237], v[202:203], off
	global_load_dwordx4 v[238:241], v[202:203], off offset:1024
	global_load_dwordx4 v[242:245], v[202:203], off offset:2048
	global_load_dwordx4 v[246:249], v[202:203], off offset:3072
	s_add_i32 s1, s0, 2
	s_mul_i32 s18, s1, 0x24000
	s_add_i32 s18, s18, 0x1000
	v_xor_b32_e32 v252, v178, v181
	v_lshl_add_u32 v252, v252, 4, v212
	v_add_u32_e32 v253, 0x10000, v252
	v_lshl_add_u64 v[250:251], v[200:201], 0, s[18:19]
	s_waitcnt vmcnt(15) lgkmcnt(3)
	v_mfma_f32_16x16x32_bf16 v[126:129], v[130:133], v[174:177], 0
	s_waitcnt lgkmcnt(2)
	v_mfma_f32_16x16x32_bf16 v[110:113], v[130:133], v[170:173], 0
	s_waitcnt vmcnt(14)
	v_mfma_f32_16x16x32_bf16 v[118:121], v[134:137], v[174:177], 0
	v_mfma_f32_16x16x32_bf16 v[102:105], v[134:137], v[170:173], 0
	s_waitcnt vmcnt(13)
	v_mfma_f32_16x16x32_bf16 v[114:117], v[138:141], v[174:177], 0
	v_mfma_f32_16x16x32_bf16 v[98:101], v[138:141], v[170:173], 0
	s_waitcnt vmcnt(12)
	v_mfma_f32_16x16x32_bf16 v[122:125], v[142:145], v[174:177], 0
	v_mfma_f32_16x16x32_bf16 v[106:109], v[142:145], v[170:173], 0
	s_waitcnt vmcnt(11)
	v_mfma_f32_16x16x32_bf16 v[62:65], v[158:161], v[174:177], 0
	v_mfma_f32_16x16x32_bf16 v[46:49], v[158:161], v[170:173], 0
	s_waitcnt vmcnt(10)
	v_mfma_f32_16x16x32_bf16 v[54:57], v[154:157], v[174:177], 0
	v_mfma_f32_16x16x32_bf16 v[38:41], v[154:157], v[170:173], 0
	s_waitcnt vmcnt(9)
	v_mfma_f32_16x16x32_bf16 v[50:53], v[150:153], v[174:177], 0
	v_mfma_f32_16x16x32_bf16 v[34:37], v[150:153], v[170:173], 0
	s_waitcnt vmcnt(8)
	v_mfma_f32_16x16x32_bf16 v[58:61], v[146:149], v[174:177], 0
	v_mfma_f32_16x16x32_bf16 v[42:45], v[146:149], v[170:173], 0
	s_waitcnt lgkmcnt(1)
	v_mfma_f32_16x16x32_bf16 v[94:97], v[130:133], v[166:169], 0
	s_waitcnt lgkmcnt(0)
; #define LOADB(dst, ks_) do { const unsigned char* ub_ = wb + (size_t)((ks_) * 144) * 1024; \
;         _Pragma("unroll") for (int j_ = 0; j_ < 8; ++j_) dst[j_] = *(const bf16x8*)(ub_ + j_ * 1024 + voff); } while (0)
; #define LOADA(fd, ks_) do { _Pragma("unroll") for (int mi_ = 0; mi_ < 4; ++mi_) fd[mi_] = AFRAG(mi_, ks_); } while (0)
; #define MMA(src, fs, ksn_) do { _Pragma("unroll") for (int mi_ = 0; mi_ < 4; ++mi_) { \
;         _Pragma("unroll") for (int j_ = 0; j_ < 8; ++j_) acc[j_][mi_] = __builtin_amdgcn_mfma_f32_16x16x32_bf16(src[j_], fs[mi_], acc[j_][mi_], 0, 0, 0); \
;         fs[mi_] = AFRAG(mi_, (ksn_) < 32 ? (ksn_) : 31); } } while (0)
; #define LOADB(dst, ks_) do { const unsigned char* ub_ = wb + (size_t)((ks_) * 64) * 1024; \
;         _Pragma("unroll") for (int j_ = 0; j_ < 8; ++j_) dst[j_] = *(const bf16x8*)(ub_ + j_ * 1024 + voff); } while (0)
; #define LOADA(fd, ks_) do { _Pragma("unroll") for (int mi_ = 0; mi_ < 4; ++mi_) fd[mi_] = AFRAG(mi_, ks_); } while (0)
; #define MMA(src, fs, ksn_) do { _Pragma("unroll") for (int mi_ = 0; mi_ < 4; ++mi_) { \
;         _Pragma("unroll") for (int j_ = 0; j_ < 8; ++j_) acc[j_][mi_] = __builtin_amdgcn_mfma_f32_16x16x32_bf16(src[j_], fs[mi_], acc[j_][mi_], 0, 0, 0); \
;         fs[mi_] = AFRAG(mi_, (ksn_) < 32 ? (ksn_) : 31); } } while (0)
; DEVINL void phase2(const Params& P, unsigned char* smem, XPre& X, const bool have_pre) {
;     ...
;                 bf16x8 fa[4];
;                 LOADB(b0, 0); LOADA(fa, 0);
; #pragma unroll 1
;                 for (int ks = 0; ks < 32; ks += 2) {
;                     LOADB(b1, ks + 1);
;                     __builtin_amdgcn_sched_barrier(0);
;                     MMA(b0, fa, ks + 1);
;                     __builtin_amdgcn_sched_barrier(0);
;                     LOADB(b0, ks + 2 < 32 ? ks + 2 : 31);
;                     __builtin_amdgcn_sched_barrier(0);
;                     MMA(b1, fa, ks + 2);
	v_mfma_f32_16x16x32_bf16 v[78:81], v[130:133], v[162:165], 0
	global_load_dwordx4 v[130:133], v[250:251], off offset:-4096
	v_mfma_f32_16x16x32_bf16 v[90:93], v[134:137], v[166:169], 0
	v_mfma_f32_16x16x32_bf16 v[74:77], v[134:137], v[162:165], 0
	global_load_dwordx4 v[134:137], v[250:251], off offset:-3072
	ds_read_b128 v[174:177], v252
	v_mfma_f32_16x16x32_bf16 v[82:85], v[138:141], v[166:169], 0
	v_mfma_f32_16x16x32_bf16 v[66:69], v[138:141], v[162:165], 0
	global_load_dwordx4 v[138:141], v[250:251], off offset:-2048
	ds_read_b128 v[170:173], v252 offset:32768
	v_mfma_f32_16x16x32_bf16 v[86:89], v[142:145], v[166:169], 0
	v_mfma_f32_16x16x32_bf16 v[70:73], v[142:145], v[162:165], 0
	global_load_dwordx4 v[142:145], v[250:251], off offset:-1024
	v_mfma_f32_16x16x32_bf16 v[30:33], v[158:161], v[166:169], 0
	v_mfma_f32_16x16x32_bf16 v[14:17], v[158:161], v[162:165], 0
	global_load_dwordx4 v[158:161], v[250:251], off
	v_mfma_f32_16x16x32_bf16 v[22:25], v[154:157], v[166:169], 0
	v_mfma_f32_16x16x32_bf16 v[10:13], v[154:157], v[162:165], 0
	global_load_dwordx4 v[154:157], v[250:251], off offset:1024
	v_mfma_f32_16x16x32_bf16 v[18:21], v[150:153], v[166:169], 0
	v_mfma_f32_16x16x32_bf16 v[2:5], v[150:153], v[162:165], 0
	global_load_dwordx4 v[150:153], v[250:251], off offset:2048
	v_mfma_f32_16x16x32_bf16 v[26:29], v[146:149], v[166:169], 0
	v_mfma_f32_16x16x32_bf16 v[6:9], v[146:149], v[162:165], 0
	global_load_dwordx4 v[146:149], v[250:251], off offset:3072
	ds_read_b128 v[166:169], v253
	ds_read_b128 v[162:165], v253 offset:32768
	s_mov_b64 s[6:7], 0x48000
	v_lshl_add_u32 v252, s1, 2, v211
	v_lshl_add_u64 v[202:203], v[202:203], 0, s[6:7]
	v_xor_b32_e32 v252, v252, v181
	v_lshl_add_u32 v252, v252, 4, v212
	v_add_u32_e32 v253, 0x10000, v252
	s_waitcnt vmcnt(15) lgkmcnt(3)
	v_mfma_f32_16x16x32_bf16 v[126:129], v[218:221], v[174:177], v[126:129]
	s_waitcnt lgkmcnt(2)
	v_mfma_f32_16x16x32_bf16 v[110:113], v[218:221], v[170:173], v[110:113]
	s_waitcnt vmcnt(14)
	v_mfma_f32_16x16x32_bf16 v[118:121], v[222:225], v[174:177], v[118:121]
	v_mfma_f32_16x16x32_bf16 v[102:105], v[222:225], v[170:173], v[102:105]
	s_waitcnt vmcnt(13)
	v_mfma_f32_16x16x32_bf16 v[114:117], v[226:229], v[174:177], v[114:117]
	v_mfma_f32_16x16x32_bf16 v[98:101], v[226:229], v[170:173], v[98:101]
	s_waitcnt vmcnt(12)
	v_mfma_f32_16x16x32_bf16 v[122:125], v[230:233], v[174:177], v[122:125]
	v_mfma_f32_16x16x32_bf16 v[106:109], v[230:233], v[170:173], v[106:109]
	s_waitcnt vmcnt(11)
	v_mfma_f32_16x16x32_bf16 v[62:65], v[234:237], v[174:177], v[62:65]
	v_mfma_f32_16x16x32_bf16 v[46:49], v[234:237], v[170:173], v[46:49]
	s_waitcnt vmcnt(10)
	v_mfma_f32_16x16x32_bf16 v[54:57], v[238:241], v[174:177], v[54:57]
	v_mfma_f32_16x16x32_bf16 v[38:41], v[238:241], v[170:173], v[38:41]
	s_waitcnt vmcnt(9)
	v_mfma_f32_16x16x32_bf16 v[50:53], v[242:245], v[174:177], v[50:53]
	v_mfma_f32_16x16x32_bf16 v[34:37], v[242:245], v[170:173], v[34:37]
	s_waitcnt vmcnt(8)
	v_mfma_f32_16x16x32_bf16 v[58:61], v[246:249], v[174:177], v[58:61]
	v_mfma_f32_16x16x32_bf16 v[42:45], v[246:249], v[170:173], v[42:45]
	s_waitcnt lgkmcnt(1)
	v_mfma_f32_16x16x32_bf16 v[94:97], v[218:221], v[166:169], v[94:97]
	s_waitcnt lgkmcnt(0)
	v_mfma_f32_16x16x32_bf16 v[78:81], v[218:221], v[162:165], v[78:81]
	global_load_dwordx4 v[218:221], v[202:203], off offset:-4096
	v_mfma_f32_16x16x32_bf16 v[90:93], v[222:225], v[166:169], v[90:93]
	v_mfma_f32_16x16x32_bf16 v[74:77], v[222:225], v[162:165], v[74:77]
	global_load_dwordx4 v[222:225], v[202:203], off offset:-3072
	ds_read_b128 v[174:177], v252
	v_mfma_f32_16x16x32_bf16 v[82:85], v[226:229], v[166:169], v[82:85]
	v_mfma_f32_16x16x32_bf16 v[66:69], v[226:229], v[162:165], v[66:69]
	global_load_dwordx4 v[226:229], v[202:203], off offset:-2048
	ds_read_b128 v[170:173], v252 offset:32768
	v_mfma_f32_16x16x32_bf16 v[86:89], v[230:233], v[166:169], v[86:89]
	v_mfma_f32_16x16x32_bf16 v[70:73], v[230:233], v[162:165], v[70:73]
	global_load_dwordx4 v[230:233], v[202:203], off offset:-1024
	v_mfma_f32_16x16x32_bf16 v[30:33], v[234:237], v[166:169], v[30:33]
	v_mfma_f32_16x16x32_bf16 v[14:17], v[234:237], v[162:165], v[14:17]
	global_load_dwordx4 v[234:237], v[202:203], off
	v_mfma_f32_16x16x32_bf16 v[22:25], v[238:241], v[166:169], v[22:25]
	v_mfma_f32_16x16x32_bf16 v[10:13], v[238:241], v[162:165], v[10:13]
	global_load_dwordx4 v[238:241], v[202:203], off offset:1024
	v_mfma_f32_16x16x32_bf16 v[18:21], v[242:245], v[166:169], v[18:21]
	v_mfma_f32_16x16x32_bf16 v[2:5], v[242:245], v[162:165], v[2:5]
	global_load_dwordx4 v[242:245], v[202:203], off offset:2048
	v_mfma_f32_16x16x32_bf16 v[26:29], v[246:249], v[166:169], v[26:29]
	v_mfma_f32_16x16x32_bf16 v[6:9], v[246:249], v[162:165], v[6:9]
	global_load_dwordx4 v[246:249], v[202:203], off offset:3072
	ds_read_b128 v[166:169], v253
	ds_read_b128 v[162:165], v253 offset:32768
	v_add_u32_e32 v178, 8, v178
	s_mov_b32 s0, s1
